# all-in combination + P8 epilogue x4 folded into the row scale (bit-identical, 128 fewer VALU per lane per tile)
# speedup vs baseline: 1.0185x; 1.0068x over previous
;     __device__ __forceinline__ void operator()(const f32x4 (&acc)[2][2][4][2], const Unit& u, int wr, int wc, int fr, int fq) const {
;     ...
;             for (int m = 0; m < 4; ++m) {
;                 const int row = row0 + ai * HALF + m * 16;
;                 const float rs = rsqrtf(ss[row] * (1.0f / 4096.0f) + RMS_EPS) * (1.0f / 64.0f);
;                 unsigned char* rowp = U + ((size_t)(row >> 4) * 512 + (col0 >> 5)) * 512 + (row & 15) * 32 + (col0 & 31);
; #pragma unroll
;                 for (int bj = 0; bj < 2; ++bj) {
;                     f32x4 v0 = acc[ai][bj][m][0] * rs, v1 = acc[ai][bj][m][1] * rs;
; #pragma unroll
;                     for (int j = 0; j < 4; ++j) { const float a = fmaxf(v0[j], 0.f), b = fmaxf(v1[j], 0.f); v0[j] = a * a * 4.f; v1[j] = b * b * 4.f; }
;                     u32x2 w; w.x = pk4_fp8(v0[0], v0[1], v0[2], v0[3]); w.y = pk4_fp8(v1[0], v1[1], v1[2], v1[3]);
;                     *(u32x2*)(rowp + bj * (HALF / 32) * 512) = w;
;                 }
.LBB0_2284:
	s_lshl_b32 s13, s20, 8
	s_add_i32 s13, s13, s36
	v_or_b32_e32 v2, s13, v1
	v_ashrrev_i32_e32 v3, 31, v2
	s_nop 15
	s_nop 15
	v_lshl_add_u64 v[4:5], v[2:3], 2, s[2:3]
	s_lshl_b32 s15, s21, 8
	s_or_b32 s15, s15, s37
	v_mov_b32_e32 v6, 0
	v_mov_b32_e32 v7, 0
	s_ashr_i32 s20, s15, 5
	s_ashr_i32 s22, s13, 4
	v_mov_b32_e32 v8, 0
	s_ashr_i32 s21, s20, 31
	s_ashr_i32 s23, s22, 31
	s_lshl_b64 s[20:21], s[20:21], 9
	s_lshl_b64 s[22:23], s[22:23], 18
	v_readlane_b32 s24, v253, 46
	v_readlane_b32 s25, v253, 47
	s_add_u32 s13, s24, s22
	s_addc_u32 s15, s25, s23
	s_add_u32 s22, s13, s20
	s_addc_u32 s23, s15, s21
	s_waitcnt vmcnt(0)
	v_fmamk_f32 v3, v234, 0x39800000, v194
	v_mul_f32_e32 v9, 0x4b800000, v3
	v_cmp_gt_f32_e32 vcc, s43, v3
	s_nop 1
	v_cndmask_b32_e32 v3, v3, v9, vcc
	v_rsq_f32_e32 v3, v3
	s_nop 0
	v_mul_f32_e32 v9, 0x45800000, v3
	v_cndmask_b32_e32 v3, v3, v9, vcc
	v_mul_f32_e32 v10, 0x3d000000, v3
	v_pk_mul_f32 v[14:15], v[158:159], v[10:11] op_sel_hi:[1,0]
	v_pk_mul_f32 v[18:19], v[154:155], v[10:11] op_sel_hi:[1,0]
	v_pk_mul_f32 v[12:13], v[160:161], v[10:11] op_sel_hi:[1,0]
	v_pk_mul_f32 v[16:17], v[156:157], v[10:11] op_sel_hi:[1,0]
	v_pk_mul_f32 v[20:21], v[152:153], v[10:11] op_sel_hi:[1,0]
	v_pk_mul_f32 v[22:23], v[150:151], v[10:11] op_sel_hi:[1,0]
	v_pk_mul_f32 v[24:25], v[148:149], v[10:11] op_sel_hi:[1,0]
	v_pk_mul_f32 v[10:11], v[146:147], v[10:11] op_sel_hi:[1,0]
	v_max_f32_e32 v3, 0, v14
	v_max_f32_e32 v9, 0, v18
	v_max_f32_e32 v14, 0, v15
	v_max_f32_e32 v15, 0, v19
	v_max_f32_e32 v18, 0, v22
	v_max_f32_e32 v10, 0, v10
	v_max_f32_e32 v19, 0, v23
	v_max_f32_e32 v11, 0, v11
	v_mul_f32_e32 v3, v3, v3
	v_mul_f32_e32 v9, v9, v9
	v_mul_f32_e32 v14, v14, v14
	v_mul_f32_e32 v15, v15, v15
	v_mul_f32_e32 v18, v18, v18
	v_mul_f32_e32 v10, v10, v10
	v_mul_f32_e32 v19, v19, v19
	v_mul_f32_e32 v11, v11, v11
	v_med3_f32 v3, v3, s44, v195
	v_med3_f32 v14, v14, s44, v195
	v_med3_f32 v9, v9, s44, v195
	v_med3_f32 v15, v15, s44, v195
	v_max_f32_e32 v12, 0, v12
	v_max_f32_e32 v16, 0, v16
	v_max_f32_e32 v13, 0, v13
	v_max_f32_e32 v17, 0, v17
	v_med3_f32 v18, v18, s44, v195
	v_med3_f32 v19, v19, s44, v195
	v_med3_f32 v10, v10, s44, v195
	v_cvt_pk_fp8_f32 v6, v3, v14
	v_cvt_pk_fp8_f32 v7, v9, v15
	v_med3_f32 v3, v11, s44, v195
	v_mov_b32_e32 v9, 0
	v_max_f32_e32 v20, 0, v20
	v_max_f32_e32 v22, 0, v24
	v_max_f32_e32 v21, 0, v21
	v_max_f32_e32 v23, 0, v25
	v_mul_f32_e32 v12, v12, v12
	v_mul_f32_e32 v16, v16, v16
	v_mul_f32_e32 v13, v13, v13
	v_mul_f32_e32 v17, v17, v17
	v_cvt_pk_fp8_f32 v8, v18, v19
	v_cvt_pk_fp8_f32 v9, v10, v3
	v_mul_f32_e32 v20, v20, v20
	v_mul_f32_e32 v22, v22, v22
	v_mul_f32_e32 v21, v21, v21
	v_mul_f32_e32 v23, v23, v23
	v_med3_f32 v12, v12, s44, v195
	v_med3_f32 v13, v13, s44, v195
	v_med3_f32 v16, v16, s44, v195
	v_med3_f32 v17, v17, s44, v195
	v_med3_f32 v20, v20, s44, v195
	v_med3_f32 v21, v21, s44, v195
	v_cvt_pk_fp8_f32 v6, v12, v13 op_sel:[0,0,1]
	v_cvt_pk_fp8_f32 v7, v16, v17 op_sel:[0,0,1]
	v_med3_f32 v3, v22, s44, v195
	v_med3_f32 v10, v23, s44, v195
	v_cvt_pk_fp8_f32 v8, v20, v21 op_sel:[0,0,1]
	v_cvt_pk_fp8_f32 v9, v3, v10 op_sel:[0,0,1]
	v_lshl_add_u64 v[10:11], s[22:23], 0, v[172:173]
	v_lshl_add_u64 v[10:11], v[10:11], 0, v[170:171]
	global_store_dwordx2 v[10:11], v[6:7], off
	global_store_dwordx2 v[10:11], v[8:9], off offset:2048
	v_or_b32_e32 v6, 16, v2
	v_ashrrev_i32_e32 v7, 31, v6
	v_lshl_add_u64 v[8:9], v[6:7], 2, s[2:3]
	v_mov_b32_e32 v8, 0
	v_mov_b32_e32 v9, 0
	v_mov_b32_e32 v10, 0
	v_ashrrev_i32_e32 v6, 4, v6
	v_ashrrev_i32_e32 v7, 31, v6
	v_lshlrev_b64 v[6:7], 18, v[6:7]
	v_lshl_add_u64 v[6:7], s[24:25], 0, v[6:7]
	v_lshl_add_u64 v[6:7], v[6:7], 0, s[20:21]
	v_lshl_add_u64 v[6:7], v[6:7], 0, v[172:173]
	v_lshl_add_u64 v[6:7], v[6:7], 0, v[170:171]
	v_fmamk_f32 v3, v235, 0x39800000, v194
	v_mul_f32_e32 v11, 0x4b800000, v3
	v_cmp_gt_f32_e32 vcc, s43, v3
	s_nop 1
	v_cndmask_b32_e32 v3, v3, v11, vcc
	v_rsq_f32_e32 v3, v3
	s_nop 0
	v_mul_f32_e32 v11, 0x45800000, v3
	v_cndmask_b32_e32 v3, v3, v11, vcc
	v_mul_f32_e32 v12, 0x3d000000, v3
	v_pk_mul_f32 v[16:17], v[142:143], v[12:13] op_sel_hi:[1,0]
	v_pk_mul_f32 v[20:21], v[138:139], v[12:13] op_sel_hi:[1,0]
	v_pk_mul_f32 v[14:15], v[144:145], v[12:13] op_sel_hi:[1,0]
	v_pk_mul_f32 v[18:19], v[140:141], v[12:13] op_sel_hi:[1,0]
	v_pk_mul_f32 v[22:23], v[136:137], v[12:13] op_sel_hi:[1,0]
	v_pk_mul_f32 v[24:25], v[134:135], v[12:13] op_sel_hi:[1,0]
	v_pk_mul_f32 v[26:27], v[132:133], v[12:13] op_sel_hi:[1,0]
	v_pk_mul_f32 v[12:13], v[130:131], v[12:13] op_sel_hi:[1,0]
	v_max_f32_e32 v3, 0, v16
	v_max_f32_e32 v11, 0, v20
	v_max_f32_e32 v16, 0, v17
	v_max_f32_e32 v17, 0, v21
	v_max_f32_e32 v20, 0, v24
	v_max_f32_e32 v12, 0, v12
	v_max_f32_e32 v21, 0, v25
	v_max_f32_e32 v13, 0, v13
	v_mul_f32_e32 v3, v3, v3
	v_mul_f32_e32 v11, v11, v11
	v_mul_f32_e32 v16, v16, v16
	v_mul_f32_e32 v17, v17, v17
	v_mul_f32_e32 v20, v20, v20
	v_mul_f32_e32 v12, v12, v12
	v_mul_f32_e32 v21, v21, v21
	v_mul_f32_e32 v13, v13, v13
	v_med3_f32 v3, v3, s44, v195
	v_med3_f32 v16, v16, s44, v195
	v_med3_f32 v11, v11, s44, v195
	v_med3_f32 v17, v17, s44, v195
	v_max_f32_e32 v14, 0, v14
	v_max_f32_e32 v18, 0, v18
	v_max_f32_e32 v15, 0, v15
	v_max_f32_e32 v19, 0, v19
	v_med3_f32 v20, v20, s44, v195
	v_med3_f32 v21, v21, s44, v195
	v_cvt_pk_fp8_f32 v8, v3, v16
	v_cvt_pk_fp8_f32 v9, v11, v17
	v_med3_f32 v3, v12, s44, v195
	v_med3_f32 v12, v13, s44, v195
	v_mov_b32_e32 v11, 0
	v_max_f32_e32 v22, 0, v22
	v_max_f32_e32 v24, 0, v26
	v_max_f32_e32 v23, 0, v23
	v_max_f32_e32 v25, 0, v27
	v_mul_f32_e32 v14, v14, v14
	v_mul_f32_e32 v18, v18, v18
	v_mul_f32_e32 v15, v15, v15
	v_mul_f32_e32 v19, v19, v19
;     __device__ __forceinline__ void operator()(const f32x4 (&acc)[2][2][4][2], const Unit& u, int wr, int wc, int fr, int fq) const {
;     ...
;             for (int m = 0; m < 4; ++m) {
;                 const int row = row0 + ai * HALF + m * 16;
;                 const float rs = rsqrtf(ss[row] * (1.0f / 4096.0f) + RMS_EPS) * (1.0f / 64.0f);
;                 unsigned char* rowp = U + ((size_t)(row >> 4) * 512 + (col0 >> 5)) * 512 + (row & 15) * 32 + (col0 & 31);
; #pragma unroll
;                 for (int bj = 0; bj < 2; ++bj) {
;                     f32x4 v0 = acc[ai][bj][m][0] * rs, v1 = acc[ai][bj][m][1] * rs;
; #pragma unroll
;                     for (int j = 0; j < 4; ++j) { const float a = fmaxf(v0[j], 0.f), b = fmaxf(v1[j], 0.f); v0[j] = a * a * 4.f; v1[j] = b * b * 4.f; }
;                     u32x2 w; w.x = pk4_fp8(v0[0], v0[1], v0[2], v0[3]); w.y = pk4_fp8(v1[0], v1[1], v1[2], v1[3]);
;                     *(u32x2*)(rowp + bj * (HALF / 32) * 512) = w;
;                 }
	v_cvt_pk_fp8_f32 v10, v20, v21
	v_cvt_pk_fp8_f32 v11, v3, v12
	v_mul_f32_e32 v22, v22, v22
	v_mul_f32_e32 v24, v24, v24
	v_mul_f32_e32 v23, v23, v23
	v_mul_f32_e32 v25, v25, v25
	v_med3_f32 v14, v14, s44, v195
	v_med3_f32 v15, v15, s44, v195
	v_med3_f32 v18, v18, s44, v195
	v_med3_f32 v19, v19, s44, v195
	v_med3_f32 v22, v22, s44, v195
	v_med3_f32 v23, v23, s44, v195
	v_cvt_pk_fp8_f32 v8, v14, v15 op_sel:[0,0,1]
	v_cvt_pk_fp8_f32 v9, v18, v19 op_sel:[0,0,1]
	v_med3_f32 v3, v24, s44, v195
	v_med3_f32 v12, v25, s44, v195
	v_cvt_pk_fp8_f32 v10, v22, v23 op_sel:[0,0,1]
	v_cvt_pk_fp8_f32 v11, v3, v12 op_sel:[0,0,1]
	global_store_dwordx2 v[6:7], v[8:9], off
	global_store_dwordx2 v[6:7], v[10:11], off offset:2048
	v_or_b32_e32 v6, 32, v2
	v_ashrrev_i32_e32 v7, 31, v6
	v_lshl_add_u64 v[8:9], v[6:7], 2, s[2:3]
	v_mov_b32_e32 v8, 0
	v_mov_b32_e32 v9, 0
	v_mov_b32_e32 v10, 0
	v_ashrrev_i32_e32 v6, 4, v6
	v_ashrrev_i32_e32 v7, 31, v6
	v_lshlrev_b64 v[6:7], 18, v[6:7]
	v_lshl_add_u64 v[6:7], s[24:25], 0, v[6:7]
	v_lshl_add_u64 v[6:7], v[6:7], 0, s[20:21]
	v_lshl_add_u64 v[6:7], v[6:7], 0, v[172:173]
	v_lshl_add_u64 v[6:7], v[6:7], 0, v[170:171]
	v_fmamk_f32 v3, v236, 0x39800000, v194
	v_mul_f32_e32 v11, 0x4b800000, v3
	v_cmp_gt_f32_e32 vcc, s43, v3
	s_nop 1
	v_cndmask_b32_e32 v3, v3, v11, vcc
	v_rsq_f32_e32 v3, v3
	s_nop 0
	v_mul_f32_e32 v11, 0x45800000, v3
	v_cndmask_b32_e32 v3, v3, v11, vcc
	v_mul_f32_e32 v12, 0x3d000000, v3
	v_pk_mul_f32 v[16:17], v[126:127], v[12:13] op_sel_hi:[1,0]
	v_pk_mul_f32 v[20:21], v[122:123], v[12:13] op_sel_hi:[1,0]
	v_pk_mul_f32 v[24:25], v[118:119], v[12:13] op_sel_hi:[1,0]
	v_pk_mul_f32 v[14:15], v[128:129], v[12:13] op_sel_hi:[1,0]
	v_pk_mul_f32 v[18:19], v[124:125], v[12:13] op_sel_hi:[1,0]
	v_pk_mul_f32 v[22:23], v[120:121], v[12:13] op_sel_hi:[1,0]
	v_pk_mul_f32 v[26:27], v[116:117], v[12:13] op_sel_hi:[1,0]
	v_pk_mul_f32 v[12:13], v[114:115], v[12:13] op_sel_hi:[1,0]
	v_max_f32_e32 v3, 0, v16
	v_max_f32_e32 v11, 0, v20
	v_max_f32_e32 v16, 0, v17
	v_max_f32_e32 v17, 0, v21
	v_max_f32_e32 v20, 0, v24
	v_max_f32_e32 v21, 0, v25
	v_max_f32_e32 v12, 0, v12
	v_max_f32_e32 v13, 0, v13
	v_mul_f32_e32 v3, v3, v3
	v_mul_f32_e32 v11, v11, v11
	v_mul_f32_e32 v16, v16, v16
	v_mul_f32_e32 v17, v17, v17
	v_mul_f32_e32 v20, v20, v20
	v_mul_f32_e32 v21, v21, v21
	v_mul_f32_e32 v12, v12, v12
	v_mul_f32_e32 v13, v13, v13
	v_med3_f32 v3, v3, s44, v195
	v_med3_f32 v16, v16, s44, v195
	v_med3_f32 v11, v11, s44, v195
	v_med3_f32 v17, v17, s44, v195
	v_med3_f32 v20, v20, s44, v195
	v_med3_f32 v21, v21, s44, v195
	v_max_f32_e32 v14, 0, v14
	v_max_f32_e32 v18, 0, v18
	v_max_f32_e32 v15, 0, v15
	v_max_f32_e32 v19, 0, v19
	v_max_f32_e32 v22, 0, v22
	v_max_f32_e32 v23, 0, v23
	v_cvt_pk_fp8_f32 v8, v3, v16
	v_cvt_pk_fp8_f32 v9, v11, v17
	v_cvt_pk_fp8_f32 v10, v20, v21
	v_med3_f32 v12, v12, s44, v195
	v_med3_f32 v13, v13, s44, v195
	v_mov_b32_e32 v11, 0
	v_max_f32_e32 v24, 0, v26
	v_max_f32_e32 v25, 0, v27
	v_mul_f32_e32 v14, v14, v14
	v_mul_f32_e32 v18, v18, v18
	v_mul_f32_e32 v15, v15, v15
	v_mul_f32_e32 v19, v19, v19
	v_mul_f32_e32 v22, v22, v22
	v_mul_f32_e32 v23, v23, v23
	v_cvt_pk_fp8_f32 v11, v12, v13
	v_mul_f32_e32 v24, v24, v24
	v_mul_f32_e32 v25, v25, v25
	v_med3_f32 v14, v14, s44, v195
	v_med3_f32 v15, v15, s44, v195
	v_med3_f32 v18, v18, s44, v195
	v_med3_f32 v19, v19, s44, v195
	v_med3_f32 v22, v22, s44, v195
	v_med3_f32 v3, v23, s44, v195
	v_cvt_pk_fp8_f32 v8, v14, v15 op_sel:[0,0,1]
	v_cvt_pk_fp8_f32 v9, v18, v19 op_sel:[0,0,1]
	v_cvt_pk_fp8_f32 v10, v22, v3 op_sel:[0,0,1]
	v_med3_f32 v3, v24, s44, v195
	v_med3_f32 v12, v25, s44, v195
	v_cvt_pk_fp8_f32 v11, v3, v12 op_sel:[0,0,1]
	global_store_dwordx2 v[6:7], v[8:9], off
	global_store_dwordx2 v[6:7], v[10:11], off offset:2048
	v_or_b32_e32 v6, 48, v2
	v_ashrrev_i32_e32 v7, 31, v6
	v_lshl_add_u64 v[8:9], v[6:7], 2, s[2:3]
	v_mov_b32_e32 v8, 0
	v_mov_b32_e32 v9, 0
	v_mov_b32_e32 v10, 0
	v_ashrrev_i32_e32 v6, 4, v6
	v_ashrrev_i32_e32 v7, 31, v6
	v_lshlrev_b64 v[6:7], 18, v[6:7]
	v_lshl_add_u64 v[6:7], s[24:25], 0, v[6:7]
	v_lshl_add_u64 v[6:7], v[6:7], 0, s[20:21]
	v_lshl_add_u64 v[6:7], v[6:7], 0, v[172:173]
	v_lshl_add_u64 v[6:7], v[6:7], 0, v[170:171]
	v_fmamk_f32 v3, v237, 0x39800000, v194
	v_mul_f32_e32 v11, 0x4b800000, v3
	v_cmp_gt_f32_e32 vcc, s43, v3
	s_nop 1
	v_cndmask_b32_e32 v3, v3, v11, vcc
	v_rsq_f32_e32 v3, v3
	s_nop 0
	v_mul_f32_e32 v11, 0x45800000, v3
	v_cndmask_b32_e32 v3, v3, v11, vcc
	v_mul_f32_e32 v12, 0x3d000000, v3
	v_pk_mul_f32 v[16:17], v[110:111], v[12:13] op_sel_hi:[1,0]
	v_pk_mul_f32 v[20:21], v[106:107], v[12:13] op_sel_hi:[1,0]
	v_pk_mul_f32 v[24:25], v[102:103], v[12:13] op_sel_hi:[1,0]
	v_pk_mul_f32 v[14:15], v[112:113], v[12:13] op_sel_hi:[1,0]
	v_pk_mul_f32 v[18:19], v[108:109], v[12:13] op_sel_hi:[1,0]
	v_pk_mul_f32 v[22:23], v[104:105], v[12:13] op_sel_hi:[1,0]
	v_pk_mul_f32 v[26:27], v[100:101], v[12:13] op_sel_hi:[1,0]
	v_pk_mul_f32 v[12:13], v[98:99], v[12:13] op_sel_hi:[1,0]
	v_max_f32_e32 v3, 0, v16
	v_max_f32_e32 v11, 0, v20
	v_max_f32_e32 v16, 0, v17
	v_max_f32_e32 v17, 0, v21
	v_max_f32_e32 v20, 0, v24
	v_max_f32_e32 v21, 0, v25
	v_max_f32_e32 v12, 0, v12
	v_max_f32_e32 v13, 0, v13
	v_mul_f32_e32 v3, v3, v3
	v_mul_f32_e32 v11, v11, v11
	v_mul_f32_e32 v16, v16, v16
	v_mul_f32_e32 v17, v17, v17
	v_mul_f32_e32 v20, v20, v20
	v_mul_f32_e32 v21, v21, v21
	v_mul_f32_e32 v12, v12, v12
	v_mul_f32_e32 v13, v13, v13
	v_med3_f32 v3, v3, s44, v195
	v_med3_f32 v16, v16, s44, v195
	v_med3_f32 v11, v11, s44, v195
	v_med3_f32 v17, v17, s44, v195
	v_med3_f32 v20, v20, s44, v195
	v_med3_f32 v21, v21, s44, v195
	v_max_f32_e32 v14, 0, v14
	v_max_f32_e32 v18, 0, v18
;     __device__ __forceinline__ void operator()(const f32x4 (&acc)[2][2][4][2], const Unit& u, int wr, int wc, int fr, int fq) const {
;     ...
;             for (int m = 0; m < 4; ++m) {
;                 const int row = row0 + ai * HALF + m * 16;
;                 const float rs = rsqrtf(ss[row] * (1.0f / 4096.0f) + RMS_EPS) * (1.0f / 64.0f);
;                 unsigned char* rowp = U + ((size_t)(row >> 4) * 512 + (col0 >> 5)) * 512 + (row & 15) * 32 + (col0 & 31);
; #pragma unroll
;                 for (int bj = 0; bj < 2; ++bj) {
;                     f32x4 v0 = acc[ai][bj][m][0] * rs, v1 = acc[ai][bj][m][1] * rs;
; #pragma unroll
;                     for (int j = 0; j < 4; ++j) { const float a = fmaxf(v0[j], 0.f), b = fmaxf(v1[j], 0.f); v0[j] = a * a * 4.f; v1[j] = b * b * 4.f; }
;                     u32x2 w; w.x = pk4_fp8(v0[0], v0[1], v0[2], v0[3]); w.y = pk4_fp8(v1[0], v1[1], v1[2], v1[3]);
;                     *(u32x2*)(rowp + bj * (HALF / 32) * 512) = w;
;                 }
	v_max_f32_e32 v15, 0, v15
	v_max_f32_e32 v19, 0, v19
	v_max_f32_e32 v22, 0, v22
	v_max_f32_e32 v23, 0, v23
	v_cvt_pk_fp8_f32 v8, v3, v16
	v_cvt_pk_fp8_f32 v9, v11, v17
	v_cvt_pk_fp8_f32 v10, v20, v21
	v_med3_f32 v12, v12, s44, v195
	v_med3_f32 v13, v13, s44, v195
	v_mov_b32_e32 v11, 0
	v_max_f32_e32 v24, 0, v26
	v_max_f32_e32 v25, 0, v27
	v_mul_f32_e32 v14, v14, v14
	v_mul_f32_e32 v18, v18, v18
	v_mul_f32_e32 v15, v15, v15
	v_mul_f32_e32 v19, v19, v19
	v_mul_f32_e32 v22, v22, v22
	v_mul_f32_e32 v23, v23, v23
	v_cvt_pk_fp8_f32 v11, v12, v13
	v_mul_f32_e32 v24, v24, v24
	v_mul_f32_e32 v25, v25, v25
	v_med3_f32 v14, v14, s44, v195
	v_med3_f32 v15, v15, s44, v195
	v_med3_f32 v18, v18, s44, v195
	v_med3_f32 v19, v19, s44, v195
	v_med3_f32 v3, v22, s44, v195
	v_med3_f32 v16, v23, s44, v195
	v_cvt_pk_fp8_f32 v8, v14, v15 op_sel:[0,0,1]
	v_cvt_pk_fp8_f32 v9, v18, v19 op_sel:[0,0,1]
	v_cvt_pk_fp8_f32 v10, v3, v16 op_sel:[0,0,1]
	v_med3_f32 v3, v24, s44, v195
	v_med3_f32 v12, v25, s44, v195
	v_cvt_pk_fp8_f32 v11, v3, v12 op_sel:[0,0,1]
	global_store_dwordx2 v[6:7], v[8:9], off
	global_store_dwordx2 v[6:7], v[10:11], off offset:2048
	v_add_u32_e32 v9, 0x80, v2
	v_ashrrev_i32_e32 v10, 4, v9
	v_mov_b32_e32 v6, 0
	v_mov_b32_e32 v7, 0
	v_mov_b32_e32 v8, 0
	v_ashrrev_i32_e32 v11, 31, v10
	v_lshlrev_b64 v[10:11], 18, v[10:11]
	v_lshl_add_u64 v[10:11], s[24:25], 0, v[10:11]
	v_lshl_add_u64 v[10:11], v[10:11], 0, s[20:21]
	v_lshl_add_u64 v[10:11], v[10:11], 0, v[172:173]
	v_lshl_add_u64 v[10:11], v[10:11], 0, v[170:171]
	v_fmamk_f32 v3, v238, 0x39800000, v194
	v_mul_f32_e32 v9, 0x4b800000, v3
	v_cmp_gt_f32_e32 vcc, s43, v3
	s_nop 1
	v_cndmask_b32_e32 v3, v3, v9, vcc
	v_rsq_f32_e32 v3, v3
	s_nop 0
	v_mul_f32_e32 v9, 0x45800000, v3
	v_cndmask_b32_e32 v3, v3, v9, vcc
	v_mul_f32_e32 v12, 0x3d000000, v3
	v_pk_mul_f32 v[16:17], v[94:95], v[12:13] op_sel_hi:[1,0]
	v_pk_mul_f32 v[20:21], v[90:91], v[12:13] op_sel_hi:[1,0]
	v_pk_mul_f32 v[24:25], v[86:87], v[12:13] op_sel_hi:[1,0]
	v_pk_mul_f32 v[14:15], v[96:97], v[12:13] op_sel_hi:[1,0]
	v_pk_mul_f32 v[18:19], v[92:93], v[12:13] op_sel_hi:[1,0]
	v_pk_mul_f32 v[22:23], v[88:89], v[12:13] op_sel_hi:[1,0]
	v_pk_mul_f32 v[26:27], v[84:85], v[12:13] op_sel_hi:[1,0]
	v_pk_mul_f32 v[12:13], v[82:83], v[12:13] op_sel_hi:[1,0]
	v_max_f32_e32 v3, 0, v16
	v_max_f32_e32 v9, 0, v20
	v_max_f32_e32 v16, 0, v17
	v_max_f32_e32 v17, 0, v21
	v_max_f32_e32 v20, 0, v24
	v_max_f32_e32 v21, 0, v25
	v_max_f32_e32 v12, 0, v12
	v_max_f32_e32 v13, 0, v13
	v_mul_f32_e32 v3, v3, v3
	v_mul_f32_e32 v9, v9, v9
	v_mul_f32_e32 v16, v16, v16
	v_mul_f32_e32 v17, v17, v17
	v_mul_f32_e32 v20, v20, v20
	v_mul_f32_e32 v21, v21, v21
	v_mul_f32_e32 v12, v12, v12
	v_mul_f32_e32 v13, v13, v13
	v_med3_f32 v3, v3, s44, v195
	v_med3_f32 v16, v16, s44, v195
	v_med3_f32 v9, v9, s44, v195
	v_med3_f32 v17, v17, s44, v195
	v_med3_f32 v20, v20, s44, v195
	v_med3_f32 v21, v21, s44, v195
	v_max_f32_e32 v14, 0, v14
	v_max_f32_e32 v18, 0, v18
	v_max_f32_e32 v15, 0, v15
	v_max_f32_e32 v19, 0, v19
	v_max_f32_e32 v22, 0, v22
	v_max_f32_e32 v23, 0, v23
	v_cvt_pk_fp8_f32 v6, v3, v16
	v_cvt_pk_fp8_f32 v7, v9, v17
	v_cvt_pk_fp8_f32 v8, v20, v21
	v_med3_f32 v12, v12, s44, v195
	v_med3_f32 v13, v13, s44, v195
	v_mov_b32_e32 v9, 0
	v_max_f32_e32 v24, 0, v26
	v_max_f32_e32 v25, 0, v27
	v_mul_f32_e32 v14, v14, v14
	v_mul_f32_e32 v18, v18, v18
	v_mul_f32_e32 v15, v15, v15
	v_mul_f32_e32 v19, v19, v19
	v_mul_f32_e32 v22, v22, v22
	v_mul_f32_e32 v23, v23, v23
	v_cvt_pk_fp8_f32 v9, v12, v13
	v_mul_f32_e32 v24, v24, v24
	v_mul_f32_e32 v25, v25, v25
	v_med3_f32 v14, v14, s44, v195
	v_med3_f32 v15, v15, s44, v195
	v_med3_f32 v18, v18, s44, v195
	v_med3_f32 v19, v19, s44, v195
	v_med3_f32 v22, v22, s44, v195
	v_med3_f32 v3, v23, s44, v195
	v_cvt_pk_fp8_f32 v6, v14, v15 op_sel:[0,0,1]
	v_cvt_pk_fp8_f32 v7, v18, v19 op_sel:[0,0,1]
	v_cvt_pk_fp8_f32 v8, v22, v3 op_sel:[0,0,1]
	v_med3_f32 v3, v24, s44, v195
	v_med3_f32 v12, v25, s44, v195
	v_cvt_pk_fp8_f32 v9, v3, v12 op_sel:[0,0,1]
	global_store_dwordx2 v[10:11], v[6:7], off
	global_store_dwordx2 v[10:11], v[8:9], off offset:2048
	v_add_u32_e32 v9, 0x90, v2
	v_ashrrev_i32_e32 v10, 4, v9
	v_mov_b32_e32 v6, 0
	v_mov_b32_e32 v7, 0
	v_mov_b32_e32 v8, 0
	v_ashrrev_i32_e32 v11, 31, v10
	v_lshlrev_b64 v[10:11], 18, v[10:11]
	v_lshl_add_u64 v[10:11], s[24:25], 0, v[10:11]
	v_lshl_add_u64 v[10:11], v[10:11], 0, s[20:21]
	v_lshl_add_u64 v[10:11], v[10:11], 0, v[172:173]
	v_lshl_add_u64 v[10:11], v[10:11], 0, v[170:171]
	v_fmamk_f32 v3, v239, 0x39800000, v194
	v_mul_f32_e32 v9, 0x4b800000, v3
	v_cmp_gt_f32_e32 vcc, s43, v3
	s_nop 1
	v_cndmask_b32_e32 v3, v3, v9, vcc
	v_rsq_f32_e32 v3, v3
	s_nop 0
	v_mul_f32_e32 v9, 0x45800000, v3
	v_cndmask_b32_e32 v3, v3, v9, vcc
	v_mul_f32_e32 v12, 0x3d000000, v3
	v_pk_mul_f32 v[16:17], v[78:79], v[12:13] op_sel_hi:[1,0]
	v_pk_mul_f32 v[20:21], v[74:75], v[12:13] op_sel_hi:[1,0]
	v_pk_mul_f32 v[14:15], v[80:81], v[12:13] op_sel_hi:[1,0]
	v_pk_mul_f32 v[18:19], v[76:77], v[12:13] op_sel_hi:[1,0]
	v_pk_mul_f32 v[22:23], v[72:73], v[12:13] op_sel_hi:[1,0]
	v_pk_mul_f32 v[24:25], v[70:71], v[12:13] op_sel_hi:[1,0]
	v_pk_mul_f32 v[26:27], v[68:69], v[12:13] op_sel_hi:[1,0]
	v_pk_mul_f32 v[12:13], v[66:67], v[12:13] op_sel_hi:[1,0]
	v_max_f32_e32 v3, 0, v16
	v_max_f32_e32 v9, 0, v20
	v_max_f32_e32 v16, 0, v17
	v_max_f32_e32 v17, 0, v21
	v_max_f32_e32 v20, 0, v24
	v_max_f32_e32 v12, 0, v12
	v_max_f32_e32 v21, 0, v25
	v_max_f32_e32 v13, 0, v13
	v_mul_f32_e32 v3, v3, v3
	v_mul_f32_e32 v9, v9, v9
	v_mul_f32_e32 v16, v16, v16
	v_mul_f32_e32 v17, v17, v17
	v_mul_f32_e32 v20, v20, v20
	v_mul_f32_e32 v12, v12, v12
;     __device__ __forceinline__ void operator()(const f32x4 (&acc)[2][2][4][2], const Unit& u, int wr, int wc, int fr, int fq) const {
;     ...
;             for (int m = 0; m < 4; ++m) {
;                 const int row = row0 + ai * HALF + m * 16;
;                 const float rs = rsqrtf(ss[row] * (1.0f / 4096.0f) + RMS_EPS) * (1.0f / 64.0f);
;                 unsigned char* rowp = U + ((size_t)(row >> 4) * 512 + (col0 >> 5)) * 512 + (row & 15) * 32 + (col0 & 31);
; #pragma unroll
;                 for (int bj = 0; bj < 2; ++bj) {
;                     f32x4 v0 = acc[ai][bj][m][0] * rs, v1 = acc[ai][bj][m][1] * rs;
; #pragma unroll
;                     for (int j = 0; j < 4; ++j) { const float a = fmaxf(v0[j], 0.f), b = fmaxf(v1[j], 0.f); v0[j] = a * a * 4.f; v1[j] = b * b * 4.f; }
;                     u32x2 w; w.x = pk4_fp8(v0[0], v0[1], v0[2], v0[3]); w.y = pk4_fp8(v1[0], v1[1], v1[2], v1[3]);
;                     *(u32x2*)(rowp + bj * (HALF / 32) * 512) = w;
;                 }
	v_mul_f32_e32 v21, v21, v21
	v_mul_f32_e32 v13, v13, v13
	v_med3_f32 v3, v3, s44, v195
	v_med3_f32 v16, v16, s44, v195
	v_med3_f32 v9, v9, s44, v195
	v_med3_f32 v17, v17, s44, v195
	v_max_f32_e32 v14, 0, v14
	v_max_f32_e32 v18, 0, v18
	v_max_f32_e32 v15, 0, v15
	v_max_f32_e32 v19, 0, v19
	v_med3_f32 v20, v20, s44, v195
	v_med3_f32 v21, v21, s44, v195
	v_cvt_pk_fp8_f32 v6, v3, v16
	v_cvt_pk_fp8_f32 v7, v9, v17
	v_med3_f32 v3, v12, s44, v195
	v_med3_f32 v12, v13, s44, v195
	v_mov_b32_e32 v9, 0
	v_max_f32_e32 v22, 0, v22
	v_max_f32_e32 v24, 0, v26
	v_max_f32_e32 v23, 0, v23
	v_max_f32_e32 v25, 0, v27
	v_mul_f32_e32 v14, v14, v14
	v_mul_f32_e32 v18, v18, v18
	v_mul_f32_e32 v15, v15, v15
	v_mul_f32_e32 v19, v19, v19
	v_cvt_pk_fp8_f32 v8, v20, v21
	v_cvt_pk_fp8_f32 v9, v3, v12
	v_mul_f32_e32 v22, v22, v22
	v_mul_f32_e32 v24, v24, v24
	v_mul_f32_e32 v23, v23, v23
	v_mul_f32_e32 v25, v25, v25
	v_med3_f32 v14, v14, s44, v195
	v_med3_f32 v15, v15, s44, v195
	v_med3_f32 v18, v18, s44, v195
	v_med3_f32 v19, v19, s44, v195
	v_med3_f32 v22, v22, s44, v195
	v_med3_f32 v23, v23, s44, v195
	v_cvt_pk_fp8_f32 v6, v14, v15 op_sel:[0,0,1]
	v_cvt_pk_fp8_f32 v7, v18, v19 op_sel:[0,0,1]
	v_med3_f32 v3, v24, s44, v195
	v_med3_f32 v12, v25, s44, v195
	v_cvt_pk_fp8_f32 v8, v22, v23 op_sel:[0,0,1]
	v_cvt_pk_fp8_f32 v9, v3, v12 op_sel:[0,0,1]
	global_store_dwordx2 v[10:11], v[6:7], off
	global_store_dwordx2 v[10:11], v[8:9], off offset:2048
	v_add_u32_e32 v9, 0xa0, v2
	v_ashrrev_i32_e32 v10, 4, v9
	v_mov_b32_e32 v6, 0
	v_mov_b32_e32 v7, 0
	v_mov_b32_e32 v8, 0
	v_ashrrev_i32_e32 v11, 31, v10
	v_lshlrev_b64 v[10:11], 18, v[10:11]
	v_lshl_add_u64 v[10:11], s[24:25], 0, v[10:11]
	v_lshl_add_u64 v[10:11], v[10:11], 0, s[20:21]
	v_lshl_add_u64 v[10:11], v[10:11], 0, v[172:173]
	v_lshl_add_u64 v[10:11], v[10:11], 0, v[170:171]
	v_add_u32_e32 v2, 0xb0, v2
	v_ashrrev_i32_e32 v2, 4, v2
	v_fmamk_f32 v3, v240, 0x39800000, v194
	v_mul_f32_e32 v9, 0x4b800000, v3
	v_cmp_gt_f32_e32 vcc, s43, v3
	s_nop 1
	v_cndmask_b32_e32 v3, v3, v9, vcc
	v_rsq_f32_e32 v3, v3
	s_nop 0
	v_mul_f32_e32 v9, 0x45800000, v3
	v_cndmask_b32_e32 v3, v3, v9, vcc
	v_mul_f32_e32 v12, 0x3d000000, v3
	v_pk_mul_f32 v[16:17], v[62:63], v[12:13] op_sel_hi:[1,0]
	v_pk_mul_f32 v[20:21], v[58:59], v[12:13] op_sel_hi:[1,0]
	v_pk_mul_f32 v[14:15], v[64:65], v[12:13] op_sel_hi:[1,0]
	v_pk_mul_f32 v[18:19], v[60:61], v[12:13] op_sel_hi:[1,0]
	v_pk_mul_f32 v[22:23], v[56:57], v[12:13] op_sel_hi:[1,0]
	v_pk_mul_f32 v[24:25], v[54:55], v[12:13] op_sel_hi:[1,0]
	v_pk_mul_f32 v[26:27], v[52:53], v[12:13] op_sel_hi:[1,0]
	v_pk_mul_f32 v[12:13], v[50:51], v[12:13] op_sel_hi:[1,0]
	v_max_f32_e32 v3, 0, v16
	v_max_f32_e32 v9, 0, v20
	v_max_f32_e32 v16, 0, v17
	v_max_f32_e32 v17, 0, v21
	v_max_f32_e32 v20, 0, v24
	v_max_f32_e32 v12, 0, v12
	v_max_f32_e32 v21, 0, v25
	v_max_f32_e32 v13, 0, v13
	v_mul_f32_e32 v3, v3, v3
	v_mul_f32_e32 v9, v9, v9
	v_mul_f32_e32 v16, v16, v16
	v_mul_f32_e32 v17, v17, v17
	v_mul_f32_e32 v20, v20, v20
	v_mul_f32_e32 v12, v12, v12
	v_mul_f32_e32 v21, v21, v21
	v_mul_f32_e32 v13, v13, v13
	v_med3_f32 v3, v3, s44, v195
	v_med3_f32 v16, v16, s44, v195
	v_med3_f32 v9, v9, s44, v195
	v_med3_f32 v17, v17, s44, v195
	v_max_f32_e32 v14, 0, v14
	v_max_f32_e32 v18, 0, v18
	v_max_f32_e32 v15, 0, v15
	v_max_f32_e32 v19, 0, v19
	v_med3_f32 v20, v20, s44, v195
	v_med3_f32 v21, v21, s44, v195
	v_med3_f32 v12, v12, s44, v195
	v_cvt_pk_fp8_f32 v6, v3, v16
	v_cvt_pk_fp8_f32 v7, v9, v17
	v_med3_f32 v3, v13, s44, v195
	v_mov_b32_e32 v9, 0
	v_max_f32_e32 v22, 0, v22
	v_max_f32_e32 v24, 0, v26
	v_max_f32_e32 v23, 0, v23
	v_max_f32_e32 v25, 0, v27
	v_mul_f32_e32 v14, v14, v14
	v_mul_f32_e32 v18, v18, v18
	v_mul_f32_e32 v15, v15, v15
	v_mul_f32_e32 v19, v19, v19
; #define PG8_BAR __builtin_amdgcn_s_barrier()
; #define PG8_BAR __builtin_amdgcn_s_barrier()
;     __device__ __forceinline__ void operator()(const f32x4 (&acc)[2][2][4][2], const Unit& u, int wr, int wc, int fr, int fq) const {
;     ...
;             for (int m = 0; m < 4; ++m) {
;                 const int row = row0 + ai * HALF + m * 16;
;                 const float rs = rsqrtf(ss[row] * (1.0f / 4096.0f) + RMS_EPS) * (1.0f / 64.0f);
;                 unsigned char* rowp = U + ((size_t)(row >> 4) * 512 + (col0 >> 5)) * 512 + (row & 15) * 32 + (col0 & 31);
; #pragma unroll
;                 for (int bj = 0; bj < 2; ++bj) {
;                     f32x4 v0 = acc[ai][bj][m][0] * rs, v1 = acc[ai][bj][m][1] * rs;
; #pragma unroll
;                     for (int j = 0; j < 4; ++j) { const float a = fmaxf(v0[j], 0.f), b = fmaxf(v1[j], 0.f); v0[j] = a * a * 4.f; v1[j] = b * b * 4.f; }
;                     u32x2 w; w.x = pk4_fp8(v0[0], v0[1], v0[2], v0[3]); w.y = pk4_fp8(v1[0], v1[1], v1[2], v1[3]);
;                     *(u32x2*)(rowp + bj * (HALF / 32) * 512) = w;
;                 }
; template <class Epi, class Sched, bool ALIGN_EPI = false, bool SP2 = false>
; __device__ __forceinline__ void gemm_phase(PG8_LAS unsigned char* lds, const Gemm g, const Sched& S, const Epi& E) {
;     ...
;         if constexpr (!Epi::AFTER_DRAIN) { E(acc, cur, wr, wc, fr, fq); S.done(cur); }
;         if (!has_next) break;
; #pragma unroll
;         for (int a = 0; a < 2; ++a)
; #pragma unroll
;             for (int b = 0; b < 2; ++b)
; #pragma unroll
;                 for (int m = 0; m < 4; ++m)
; #pragma unroll
;                     for (int n = 0; n < 2; ++n) acc[a][b][m][n] = (f32x4){0.f, 0.f, 0.f, 0.f};
;         cur = nxt; cA = nA; cB = nB; ++ui;
;         if constexpr (ALIGN_EPI) { if (wr == 1) PG8_BAR; }
;     }
	v_cvt_pk_fp8_f32 v8, v20, v21
	v_cvt_pk_fp8_f32 v9, v12, v3
	v_mul_f32_e32 v22, v22, v22
	v_mul_f32_e32 v24, v24, v24
	v_mul_f32_e32 v23, v23, v23
	v_mul_f32_e32 v25, v25, v25
	v_med3_f32 v14, v14, s44, v195
	v_med3_f32 v15, v15, s44, v195
	v_med3_f32 v18, v18, s44, v195
	v_med3_f32 v19, v19, s44, v195
	v_med3_f32 v22, v22, s44, v195
	v_med3_f32 v23, v23, s44, v195
	v_cvt_pk_fp8_f32 v6, v14, v15 op_sel:[0,0,1]
	v_cvt_pk_fp8_f32 v7, v18, v19 op_sel:[0,0,1]
	v_med3_f32 v3, v24, s44, v195
	v_med3_f32 v12, v25, s44, v195
	v_cvt_pk_fp8_f32 v8, v22, v23 op_sel:[0,0,1]
	v_cvt_pk_fp8_f32 v9, v3, v12 op_sel:[0,0,1]
	global_store_dwordx2 v[10:11], v[6:7], off
	global_store_dwordx2 v[10:11], v[8:9], off offset:2048
	v_mov_b32_e32 v4, 0
	v_mov_b32_e32 v5, 0
	v_mov_b32_e32 v6, 0
	v_mov_b32_e32 v7, 0
	v_ashrrev_i32_e32 v3, 31, v2
	v_lshlrev_b64 v[2:3], 18, v[2:3]
	v_lshl_add_u64 v[2:3], s[24:25], 0, v[2:3]
	v_lshl_add_u64 v[2:3], v[2:3], 0, s[20:21]
	v_lshl_add_u64 v[2:3], v[2:3], 0, v[172:173]
	v_lshl_add_u64 v[2:3], v[2:3], 0, v[170:171]
	v_fmamk_f32 v8, v241, 0x39800000, v194
	v_mul_f32_e32 v9, 0x4b800000, v8
	v_cmp_gt_f32_e32 vcc, s43, v8
	s_nop 1
	v_cndmask_b32_e32 v8, v8, v9, vcc
	v_rsq_f32_e32 v8, v8
	s_nop 0
	v_mul_f32_e32 v9, 0x45800000, v8
	v_cndmask_b32_e32 v8, v8, v9, vcc
	v_mul_f32_e32 v8, 0x3d000000, v8
	v_pk_mul_f32 v[12:13], v[46:47], v[8:9] op_sel_hi:[1,0]
	v_pk_mul_f32 v[16:17], v[42:43], v[8:9] op_sel_hi:[1,0]
	v_pk_mul_f32 v[10:11], v[48:49], v[8:9] op_sel_hi:[1,0]
	v_pk_mul_f32 v[14:15], v[44:45], v[8:9] op_sel_hi:[1,0]
	v_pk_mul_f32 v[18:19], v[40:41], v[8:9] op_sel_hi:[1,0]
	v_pk_mul_f32 v[20:21], v[38:39], v[8:9] op_sel_hi:[1,0]
	v_pk_mul_f32 v[22:23], v[36:37], v[8:9] op_sel_hi:[1,0]
	v_pk_mul_f32 v[8:9], v[34:35], v[8:9] op_sel_hi:[1,0]
	v_max_f32_e32 v12, 0, v12
	v_max_f32_e32 v16, 0, v16
	v_max_f32_e32 v13, 0, v13
	v_max_f32_e32 v17, 0, v17
	v_max_f32_e32 v20, 0, v20
	v_max_f32_e32 v8, 0, v8
	v_max_f32_e32 v21, 0, v21
	v_max_f32_e32 v9, 0, v9
	v_mul_f32_e32 v12, v12, v12
	v_mul_f32_e32 v16, v16, v16
	v_mul_f32_e32 v13, v13, v13
	v_mul_f32_e32 v17, v17, v17
	v_mul_f32_e32 v20, v20, v20
	v_mul_f32_e32 v8, v8, v8
	v_mul_f32_e32 v21, v21, v21
	v_mul_f32_e32 v9, v9, v9
	v_med3_f32 v12, v12, s44, v195
	v_med3_f32 v13, v13, s44, v195
	v_med3_f32 v16, v16, s44, v195
	v_med3_f32 v17, v17, s44, v195
	v_max_f32_e32 v10, 0, v10
	v_max_f32_e32 v14, 0, v14
	v_max_f32_e32 v11, 0, v11
	v_max_f32_e32 v15, 0, v15
	v_med3_f32 v20, v20, s44, v195
	v_med3_f32 v21, v21, s44, v195
	v_med3_f32 v8, v8, s44, v195
	v_cvt_pk_fp8_f32 v4, v12, v13
	v_cvt_pk_fp8_f32 v5, v16, v17
	v_med3_f32 v9, v9, s44, v195
	v_max_f32_e32 v18, 0, v18
	v_max_f32_e32 v22, 0, v22
	v_max_f32_e32 v19, 0, v19
	v_max_f32_e32 v23, 0, v23
	v_mul_f32_e32 v10, v10, v10
	v_mul_f32_e32 v14, v14, v14
	v_mul_f32_e32 v11, v11, v11
	v_mul_f32_e32 v15, v15, v15
	v_cvt_pk_fp8_f32 v6, v20, v21
	v_cvt_pk_fp8_f32 v7, v8, v9
	v_mul_f32_e32 v18, v18, v18
	v_mul_f32_e32 v22, v22, v22
	v_mul_f32_e32 v19, v19, v19
	v_mul_f32_e32 v23, v23, v23
	v_med3_f32 v10, v10, s44, v195
	v_med3_f32 v11, v11, s44, v195
	v_med3_f32 v14, v14, s44, v195
	v_med3_f32 v15, v15, s44, v195
	v_med3_f32 v18, v18, s44, v195
	v_med3_f32 v19, v19, s44, v195
	v_cvt_pk_fp8_f32 v4, v10, v11 op_sel:[0,0,1]
	v_cvt_pk_fp8_f32 v5, v14, v15 op_sel:[0,0,1]
	v_med3_f32 v8, v22, s44, v195
	v_med3_f32 v9, v23, s44, v195
	v_cvt_pk_fp8_f32 v6, v18, v19 op_sel:[0,0,1]
	v_cvt_pk_fp8_f32 v7, v8, v9 op_sel:[0,0,1]
	s_andn2_b64 vcc, exec, s[0:1]
	s_mov_b64 s[0:1], -1
	global_store_dwordx2 v[2:3], v[4:5], off
	global_store_dwordx2 v[2:3], v[6:7], off offset:2048
	s_cbranch_vccnz .LBB0_2273
	s_andn2_b64 vcc, exec, s[4:5]
	s_cbranch_vccnz .LBB0_2272
	s_barrier
	s_branch .LBB0_2272
